# stack6
# speedup vs baseline: 1.0182x; 1.0182x over previous
.Lro_loaded:
	s_waitcnt vmcnt(0)
	s_mov_b32 s36, 0xffff
	s_cmp_le_u32 s14, 0
	s_cbranch_scc1 .Lro_built
	v_cmp_lt_u32_e32 vcc, s36, v32
	s_mov_b64 exec, vcc
	ds_write_b32 v9, v32 offset:0
	v_bfe_u32 v27, v32, 4, 4
	v_add_u32_e32 v6, 1, v6
	v_lshlrev_b32_e64 v28, v27, 1
	v_or_b32_e32 v7, v7, v28
	v_lshl_add_u32 v27, v27, 9, v8
	v_mov_b32_e32 v24, 1
	v_mov_b32_e32 v25, 0
	ds_or_b64 v27, v[24:25]
	s_mov_b64 exec, -1
	v_cmp_lt_u32_e32 vcc, s36, v33
	s_mov_b64 exec, vcc
	ds_write_b32 v9, v33 offset:256
	v_bfe_u32 v27, v33, 4, 4
	v_add_u32_e32 v6, 1, v6
	v_lshlrev_b32_e64 v28, v27, 1
	v_or_b32_e32 v7, v7, v28
	v_lshl_add_u32 v27, v27, 9, v8
	v_mov_b32_e32 v24, 2
	v_mov_b32_e32 v25, 0
	ds_or_b64 v27, v[24:25]
	s_mov_b64 exec, -1
	v_cmp_lt_u32_e32 vcc, s36, v34
	s_mov_b64 exec, vcc
	ds_write_b32 v9, v34 offset:512
	v_bfe_u32 v27, v34, 4, 4
	v_add_u32_e32 v6, 1, v6
	v_lshlrev_b32_e64 v28, v27, 1
	v_or_b32_e32 v7, v7, v28
	v_lshl_add_u32 v27, v27, 9, v8
	v_mov_b32_e32 v24, 4
	v_mov_b32_e32 v25, 0
	ds_or_b64 v27, v[24:25]
	s_mov_b64 exec, -1
	v_cmp_lt_u32_e32 vcc, s36, v35
	s_mov_b64 exec, vcc
	ds_write_b32 v9, v35 offset:768
	v_bfe_u32 v27, v35, 4, 4
	v_add_u32_e32 v6, 1, v6
	v_lshlrev_b32_e64 v28, v27, 1
	v_or_b32_e32 v7, v7, v28
	v_lshl_add_u32 v27, v27, 9, v8
	v_mov_b32_e32 v24, 8
	v_mov_b32_e32 v25, 0
	ds_or_b64 v27, v[24:25]
	s_mov_b64 exec, -1
	s_cmp_le_u32 s14, 4
	s_cbranch_scc1 .Lro_built
	v_cmp_lt_u32_e32 vcc, s36, v36
	s_mov_b64 exec, vcc
	ds_write_b32 v9, v36 offset:1024
	v_bfe_u32 v27, v36, 4, 4
	v_add_u32_e32 v6, 1, v6
	v_lshlrev_b32_e64 v28, v27, 1
	v_or_b32_e32 v7, v7, v28
	v_lshl_add_u32 v27, v27, 9, v8
	v_mov_b32_e32 v24, 16
	v_mov_b32_e32 v25, 0
	ds_or_b64 v27, v[24:25]
	s_mov_b64 exec, -1
	v_cmp_lt_u32_e32 vcc, s36, v37
	s_mov_b64 exec, vcc
	ds_write_b32 v9, v37 offset:1280
	v_bfe_u32 v27, v37, 4, 4
	v_add_u32_e32 v6, 1, v6
	v_lshlrev_b32_e64 v28, v27, 1
	v_or_b32_e32 v7, v7, v28
	v_lshl_add_u32 v27, v27, 9, v8
	v_mov_b32_e32 v24, 32
	v_mov_b32_e32 v25, 0
	ds_or_b64 v27, v[24:25]
	s_mov_b64 exec, -1
	v_cmp_lt_u32_e32 vcc, s36, v38
	s_mov_b64 exec, vcc
	ds_write_b32 v9, v38 offset:1536
	v_bfe_u32 v27, v38, 4, 4
	v_add_u32_e32 v6, 1, v6
	v_lshlrev_b32_e64 v28, v27, 1
	v_or_b32_e32 v7, v7, v28
	v_lshl_add_u32 v27, v27, 9, v8
	v_mov_b32_e32 v24, 64
	v_mov_b32_e32 v25, 0
	ds_or_b64 v27, v[24:25]
	s_mov_b64 exec, -1
	v_cmp_lt_u32_e32 vcc, s36, v39
	s_mov_b64 exec, vcc
	ds_write_b32 v9, v39 offset:1792
	v_bfe_u32 v27, v39, 4, 4
	v_add_u32_e32 v6, 1, v6
	v_lshlrev_b32_e64 v28, v27, 1
	v_or_b32_e32 v7, v7, v28
	v_lshl_add_u32 v27, v27, 9, v8
	v_mov_b32_e32 v24, 0x80
	v_mov_b32_e32 v25, 0
	ds_or_b64 v27, v[24:25]
	s_mov_b64 exec, -1
	s_cmp_le_u32 s14, 8
	s_cbranch_scc1 .Lro_built
	v_cmp_lt_u32_e32 vcc, s36, v40
	s_mov_b64 exec, vcc
	ds_write_b32 v9, v40 offset:2048
	v_bfe_u32 v27, v40, 4, 4
	v_add_u32_e32 v6, 1, v6
	v_lshlrev_b32_e64 v28, v27, 1
	v_or_b32_e32 v7, v7, v28
	v_lshl_add_u32 v27, v27, 9, v8
	v_mov_b32_e32 v24, 0x100
	v_mov_b32_e32 v25, 0
	ds_or_b64 v27, v[24:25]
	s_mov_b64 exec, -1
	v_cmp_lt_u32_e32 vcc, s36, v41
	s_mov_b64 exec, vcc
	ds_write_b32 v9, v41 offset:2304
	v_bfe_u32 v27, v41, 4, 4
	v_add_u32_e32 v6, 1, v6
	v_lshlrev_b32_e64 v28, v27, 1
	v_or_b32_e32 v7, v7, v28
	v_lshl_add_u32 v27, v27, 9, v8
	v_mov_b32_e32 v24, 0x200
	v_mov_b32_e32 v25, 0
	ds_or_b64 v27, v[24:25]
	s_mov_b64 exec, -1
	v_cmp_lt_u32_e32 vcc, s36, v42
	s_mov_b64 exec, vcc
	ds_write_b32 v9, v42 offset:2560
	v_bfe_u32 v27, v42, 4, 4
	v_add_u32_e32 v6, 1, v6
	v_lshlrev_b32_e64 v28, v27, 1
	v_or_b32_e32 v7, v7, v28
	v_lshl_add_u32 v27, v27, 9, v8
	v_mov_b32_e32 v24, 0x400
	v_mov_b32_e32 v25, 0
	ds_or_b64 v27, v[24:25]
	s_mov_b64 exec, -1
	v_cmp_lt_u32_e32 vcc, s36, v43
	s_mov_b64 exec, vcc
	ds_write_b32 v9, v43 offset:2816
	v_bfe_u32 v27, v43, 4, 4
	v_add_u32_e32 v6, 1, v6
	v_lshlrev_b32_e64 v28, v27, 1
	v_or_b32_e32 v7, v7, v28
	v_lshl_add_u32 v27, v27, 9, v8
	v_mov_b32_e32 v24, 0x800
	v_mov_b32_e32 v25, 0
	ds_or_b64 v27, v[24:25]
	s_mov_b64 exec, -1
	s_cmp_le_u32 s14, 12
	s_cbranch_scc1 .Lro_built
	v_cmp_lt_u32_e32 vcc, s36, v44
	s_mov_b64 exec, vcc
	ds_write_b32 v9, v44 offset:3072
	v_bfe_u32 v27, v44, 4, 4
	v_add_u32_e32 v6, 1, v6
	v_lshlrev_b32_e64 v28, v27, 1
	v_or_b32_e32 v7, v7, v28
	v_lshl_add_u32 v27, v27, 9, v8
	v_mov_b32_e32 v24, 0x1000
	v_mov_b32_e32 v25, 0
	ds_or_b64 v27, v[24:25]
	s_mov_b64 exec, -1
	v_cmp_lt_u32_e32 vcc, s36, v45
	s_mov_b64 exec, vcc
	ds_write_b32 v9, v45 offset:3328
	v_bfe_u32 v27, v45, 4, 4
	v_add_u32_e32 v6, 1, v6
	v_lshlrev_b32_e64 v28, v27, 1
	v_or_b32_e32 v7, v7, v28
	v_lshl_add_u32 v27, v27, 9, v8
	v_mov_b32_e32 v24, 0x2000
	v_mov_b32_e32 v25, 0
	ds_or_b64 v27, v[24:25]
	s_mov_b64 exec, -1
	v_cmp_lt_u32_e32 vcc, s36, v46
	s_mov_b64 exec, vcc
	ds_write_b32 v9, v46 offset:3584
	v_bfe_u32 v27, v46, 4, 4
	v_add_u32_e32 v6, 1, v6
	v_lshlrev_b32_e64 v28, v27, 1
	v_or_b32_e32 v7, v7, v28
	v_lshl_add_u32 v27, v27, 9, v8
	v_mov_b32_e32 v24, 0x4000
	v_mov_b32_e32 v25, 0
	ds_or_b64 v27, v[24:25]
	s_mov_b64 exec, -1
	v_cmp_lt_u32_e32 vcc, s36, v47
	s_mov_b64 exec, vcc
	ds_write_b32 v9, v47 offset:3840
	v_bfe_u32 v27, v47, 4, 4
	v_add_u32_e32 v6, 1, v6
	v_lshlrev_b32_e64 v28, v27, 1
	v_or_b32_e32 v7, v7, v28
	v_lshl_add_u32 v27, v27, 9, v8
	v_mov_b32_e32 v24, 0x8000
	v_mov_b32_e32 v25, 0
	ds_or_b64 v27, v[24:25]
	s_mov_b64 exec, -1
	s_cmp_le_u32 s14, 16
	s_cbranch_scc1 .Lro_built
	v_cmp_lt_u32_e32 vcc, s36, v48
	s_mov_b64 exec, vcc
	ds_write_b32 v9, v48 offset:4096
	v_bfe_u32 v27, v48, 4, 4
	v_add_u32_e32 v6, 1, v6
	v_lshlrev_b32_e64 v28, v27, 1
	v_or_b32_e32 v7, v7, v28
	v_lshl_add_u32 v27, v27, 9, v8
	v_mov_b32_e32 v24, 0x10000
	v_mov_b32_e32 v25, 0
	ds_or_b64 v27, v[24:25]
	s_mov_b64 exec, -1
	v_cmp_lt_u32_e32 vcc, s36, v49
	s_mov_b64 exec, vcc
	ds_write_b32 v9, v49 offset:4352
	v_bfe_u32 v27, v49, 4, 4
	v_add_u32_e32 v6, 1, v6
	v_lshlrev_b32_e64 v28, v27, 1
	v_or_b32_e32 v7, v7, v28
	v_lshl_add_u32 v27, v27, 9, v8
	v_mov_b32_e32 v24, 0x20000
	v_mov_b32_e32 v25, 0
	ds_or_b64 v27, v[24:25]
	s_mov_b64 exec, -1
	v_cmp_lt_u32_e32 vcc, s36, v50
	s_mov_b64 exec, vcc
	ds_write_b32 v9, v50 offset:4608
	v_bfe_u32 v27, v50, 4, 4
	v_add_u32_e32 v6, 1, v6
	v_lshlrev_b32_e64 v28, v27, 1
	v_or_b32_e32 v7, v7, v28
	v_lshl_add_u32 v27, v27, 9, v8
	v_mov_b32_e32 v24, 0x40000
	v_mov_b32_e32 v25, 0
	ds_or_b64 v27, v[24:25]
	s_mov_b64 exec, -1
	v_cmp_lt_u32_e32 vcc, s36, v51
	s_mov_b64 exec, vcc
	ds_write_b32 v9, v51 offset:4864
	v_bfe_u32 v27, v51, 4, 4
	v_add_u32_e32 v6, 1, v6
	v_lshlrev_b32_e64 v28, v27, 1
	v_or_b32_e32 v7, v7, v28
	v_lshl_add_u32 v27, v27, 9, v8
	v_mov_b32_e32 v24, 0x80000
	v_mov_b32_e32 v25, 0
	ds_or_b64 v27, v[24:25]
	s_mov_b64 exec, -1
	s_cmp_le_u32 s14, 20
	s_cbranch_scc1 .Lro_built
	v_cmp_lt_u32_e32 vcc, s36, v52
	s_mov_b64 exec, vcc
	ds_write_b32 v9, v52 offset:5120
	v_bfe_u32 v27, v52, 4, 4
	v_add_u32_e32 v6, 1, v6
	v_lshlrev_b32_e64 v28, v27, 1
	v_or_b32_e32 v7, v7, v28
	v_lshl_add_u32 v27, v27, 9, v8
	v_mov_b32_e32 v24, 0x100000
	v_mov_b32_e32 v25, 0
	ds_or_b64 v27, v[24:25]
	s_mov_b64 exec, -1
	v_cmp_lt_u32_e32 vcc, s36, v53
	s_mov_b64 exec, vcc
	ds_write_b32 v9, v53 offset:5376
	v_bfe_u32 v27, v53, 4, 4
	v_add_u32_e32 v6, 1, v6
	v_lshlrev_b32_e64 v28, v27, 1
	v_or_b32_e32 v7, v7, v28
	v_lshl_add_u32 v27, v27, 9, v8
	v_mov_b32_e32 v24, 0x200000
	v_mov_b32_e32 v25, 0
	ds_or_b64 v27, v[24:25]
	s_mov_b64 exec, -1
	v_cmp_lt_u32_e32 vcc, s36, v54
	s_mov_b64 exec, vcc
	ds_write_b32 v9, v54 offset:5632
	v_bfe_u32 v27, v54, 4, 4
	v_add_u32_e32 v6, 1, v6
	v_lshlrev_b32_e64 v28, v27, 1
	v_or_b32_e32 v7, v7, v28
	v_lshl_add_u32 v27, v27, 9, v8
	v_mov_b32_e32 v24, 0x400000
	v_mov_b32_e32 v25, 0
	ds_or_b64 v27, v[24:25]
	s_mov_b64 exec, -1
	v_cmp_lt_u32_e32 vcc, s36, v55
	s_mov_b64 exec, vcc
	ds_write_b32 v9, v55 offset:5888
	v_bfe_u32 v27, v55, 4, 4
	v_add_u32_e32 v6, 1, v6
	v_lshlrev_b32_e64 v28, v27, 1
	v_or_b32_e32 v7, v7, v28
	v_lshl_add_u32 v27, v27, 9, v8
	v_mov_b32_e32 v24, 0x800000
	v_mov_b32_e32 v25, 0
	ds_or_b64 v27, v[24:25]
	s_mov_b64 exec, -1
	s_cmp_le_u32 s14, 24
	s_cbranch_scc1 .Lro_built
	v_cmp_lt_u32_e32 vcc, s36, v56
	s_mov_b64 exec, vcc
	ds_write_b32 v9, v56 offset:6144
	v_bfe_u32 v27, v56, 4, 4
	v_add_u32_e32 v6, 1, v6
	v_lshlrev_b32_e64 v28, v27, 1
	v_or_b32_e32 v7, v7, v28
	v_lshl_add_u32 v27, v27, 9, v8
	v_mov_b32_e32 v24, 0x1000000
	v_mov_b32_e32 v25, 0
	ds_or_b64 v27, v[24:25]
	s_mov_b64 exec, -1
	v_cmp_lt_u32_e32 vcc, s36, v57
	s_mov_b64 exec, vcc
	ds_write_b32 v9, v57 offset:6400
	v_bfe_u32 v27, v57, 4, 4
	v_add_u32_e32 v6, 1, v6
	v_lshlrev_b32_e64 v28, v27, 1
	v_or_b32_e32 v7, v7, v28
	v_lshl_add_u32 v27, v27, 9, v8
	v_mov_b32_e32 v24, 0x2000000
	v_mov_b32_e32 v25, 0
	ds_or_b64 v27, v[24:25]
	s_mov_b64 exec, -1
	v_cmp_lt_u32_e32 vcc, s36, v58
	s_mov_b64 exec, vcc
	ds_write_b32 v9, v58 offset:6656
	v_bfe_u32 v27, v58, 4, 4
	v_add_u32_e32 v6, 1, v6
	v_lshlrev_b32_e64 v28, v27, 1
	v_or_b32_e32 v7, v7, v28
	v_lshl_add_u32 v27, v27, 9, v8
	v_mov_b32_e32 v24, 0x4000000
	v_mov_b32_e32 v25, 0
	ds_or_b64 v27, v[24:25]
	s_mov_b64 exec, -1
	v_cmp_lt_u32_e32 vcc, s36, v59
	s_mov_b64 exec, vcc
	ds_write_b32 v9, v59 offset:6912
	v_bfe_u32 v27, v59, 4, 4
	v_add_u32_e32 v6, 1, v6
	v_lshlrev_b32_e64 v28, v27, 1
	v_or_b32_e32 v7, v7, v28
	v_lshl_add_u32 v27, v27, 9, v8
	v_mov_b32_e32 v24, 0x8000000
	v_mov_b32_e32 v25, 0
	ds_or_b64 v27, v[24:25]
	s_mov_b64 exec, -1
	s_cmp_le_u32 s14, 28
	s_cbranch_scc1 .Lro_built
	v_cmp_lt_u32_e32 vcc, s36, v60
	s_mov_b64 exec, vcc
	ds_write_b32 v9, v60 offset:7168
	v_bfe_u32 v27, v60, 4, 4
	v_add_u32_e32 v6, 1, v6
	v_lshlrev_b32_e64 v28, v27, 1
	v_or_b32_e32 v7, v7, v28
	v_lshl_add_u32 v27, v27, 9, v8
	v_mov_b32_e32 v24, 0x10000000
	v_mov_b32_e32 v25, 0
	ds_or_b64 v27, v[24:25]
	s_mov_b64 exec, -1
	v_cmp_lt_u32_e32 vcc, s36, v61
	s_mov_b64 exec, vcc
	ds_write_b32 v9, v61 offset:7424
	v_bfe_u32 v27, v61, 4, 4
	v_add_u32_e32 v6, 1, v6
	v_lshlrev_b32_e64 v28, v27, 1
	v_or_b32_e32 v7, v7, v28
	v_lshl_add_u32 v27, v27, 9, v8
	v_mov_b32_e32 v24, 0x20000000
	v_mov_b32_e32 v25, 0
	ds_or_b64 v27, v[24:25]
	s_mov_b64 exec, -1
	v_cmp_lt_u32_e32 vcc, s36, v62
	s_mov_b64 exec, vcc
	ds_write_b32 v9, v62 offset:7680
	v_bfe_u32 v27, v62, 4, 4
	v_add_u32_e32 v6, 1, v6
	v_lshlrev_b32_e64 v28, v27, 1
	v_or_b32_e32 v7, v7, v28
	v_lshl_add_u32 v27, v27, 9, v8
	v_mov_b32_e32 v24, 0x40000000
	v_mov_b32_e32 v25, 0
	ds_or_b64 v27, v[24:25]
	s_mov_b64 exec, -1
	v_cmp_lt_u32_e32 vcc, s36, v63
	s_mov_b64 exec, vcc
	ds_write_b32 v9, v63 offset:7936
	v_bfe_u32 v27, v63, 4, 4
	v_add_u32_e32 v6, 1, v6
	v_lshlrev_b32_e64 v28, v27, 1
	v_or_b32_e32 v7, v7, v28
	v_lshl_add_u32 v27, v27, 9, v8
	v_mov_b32_e32 v24, 0x80000000
	v_mov_b32_e32 v25, 0
	ds_or_b64 v27, v[24:25]
	s_mov_b64 exec, -1
	s_cmp_le_u32 s14, 32
	s_cbranch_scc1 .Lro_built
	v_cmp_lt_u32_e32 vcc, s36, v64
	s_mov_b64 exec, vcc
	ds_write_b32 v9, v64 offset:8192
	v_bfe_u32 v27, v64, 4, 4
	v_add_u32_e32 v6, 1, v6
	v_lshlrev_b32_e64 v28, v27, 1
	v_or_b32_e32 v7, v7, v28
	v_lshl_add_u32 v27, v27, 9, v8
	v_mov_b32_e32 v24, 0
	v_mov_b32_e32 v25, 1
	ds_or_b64 v27, v[24:25]
	s_mov_b64 exec, -1
	v_cmp_lt_u32_e32 vcc, s36, v65
	s_mov_b64 exec, vcc
	ds_write_b32 v9, v65 offset:8448
	v_bfe_u32 v27, v65, 4, 4
	v_add_u32_e32 v6, 1, v6
	v_lshlrev_b32_e64 v28, v27, 1
	v_or_b32_e32 v7, v7, v28
	v_lshl_add_u32 v27, v27, 9, v8
	v_mov_b32_e32 v24, 0
	v_mov_b32_e32 v25, 2
	ds_or_b64 v27, v[24:25]
	s_mov_b64 exec, -1
	v_cmp_lt_u32_e32 vcc, s36, v66
	s_mov_b64 exec, vcc
	ds_write_b32 v9, v66 offset:8704
	v_bfe_u32 v27, v66, 4, 4
	v_add_u32_e32 v6, 1, v6
	v_lshlrev_b32_e64 v28, v27, 1
	v_or_b32_e32 v7, v7, v28
	v_lshl_add_u32 v27, v27, 9, v8
	v_mov_b32_e32 v24, 0
	v_mov_b32_e32 v25, 4
	ds_or_b64 v27, v[24:25]
	s_mov_b64 exec, -1
	v_cmp_lt_u32_e32 vcc, s36, v67
	s_mov_b64 exec, vcc
	ds_write_b32 v9, v67 offset:8960
	v_bfe_u32 v27, v67, 4, 4
	v_add_u32_e32 v6, 1, v6
	v_lshlrev_b32_e64 v28, v27, 1
	v_or_b32_e32 v7, v7, v28
	v_lshl_add_u32 v27, v27, 9, v8
	v_mov_b32_e32 v24, 0
	v_mov_b32_e32 v25, 8
	ds_or_b64 v27, v[24:25]
	s_mov_b64 exec, -1
	s_cmp_le_u32 s14, 36
	s_cbranch_scc1 .Lro_built
	v_cmp_lt_u32_e32 vcc, s36, v68
	s_mov_b64 exec, vcc
	ds_write_b32 v9, v68 offset:9216
	v_bfe_u32 v27, v68, 4, 4
	v_add_u32_e32 v6, 1, v6
	v_lshlrev_b32_e64 v28, v27, 1
	v_or_b32_e32 v7, v7, v28
	v_lshl_add_u32 v27, v27, 9, v8
	v_mov_b32_e32 v24, 0
	v_mov_b32_e32 v25, 16
	ds_or_b64 v27, v[24:25]
	s_mov_b64 exec, -1
	v_cmp_lt_u32_e32 vcc, s36, v69
	s_mov_b64 exec, vcc
	ds_write_b32 v9, v69 offset:9472
	v_bfe_u32 v27, v69, 4, 4
	v_add_u32_e32 v6, 1, v6
	v_lshlrev_b32_e64 v28, v27, 1
	v_or_b32_e32 v7, v7, v28
	v_lshl_add_u32 v27, v27, 9, v8
	v_mov_b32_e32 v24, 0
	v_mov_b32_e32 v25, 32
	ds_or_b64 v27, v[24:25]
	s_mov_b64 exec, -1
	v_cmp_lt_u32_e32 vcc, s36, v70
	s_mov_b64 exec, vcc
	ds_write_b32 v9, v70 offset:9728
	v_bfe_u32 v27, v70, 4, 4
	v_add_u32_e32 v6, 1, v6
	v_lshlrev_b32_e64 v28, v27, 1
	v_or_b32_e32 v7, v7, v28
	v_lshl_add_u32 v27, v27, 9, v8
	v_mov_b32_e32 v24, 0
	v_mov_b32_e32 v25, 64
	ds_or_b64 v27, v[24:25]
	s_mov_b64 exec, -1
	v_cmp_lt_u32_e32 vcc, s36, v71
	s_mov_b64 exec, vcc
	ds_write_b32 v9, v71 offset:9984
	v_bfe_u32 v27, v71, 4, 4
	v_add_u32_e32 v6, 1, v6
	v_lshlrev_b32_e64 v28, v27, 1
	v_or_b32_e32 v7, v7, v28
	v_lshl_add_u32 v27, v27, 9, v8
	v_mov_b32_e32 v24, 0
	v_mov_b32_e32 v25, 0x80
	ds_or_b64 v27, v[24:25]
	s_mov_b64 exec, -1
	s_cmp_le_u32 s14, 40
	s_cbranch_scc1 .Lro_built
	v_cmp_lt_u32_e32 vcc, s36, v72
	s_mov_b64 exec, vcc
	ds_write_b32 v9, v72 offset:10240
	v_bfe_u32 v27, v72, 4, 4
	v_add_u32_e32 v6, 1, v6
	v_lshlrev_b32_e64 v28, v27, 1
	v_or_b32_e32 v7, v7, v28
	v_lshl_add_u32 v27, v27, 9, v8
	v_mov_b32_e32 v24, 0
	v_mov_b32_e32 v25, 0x100
	ds_or_b64 v27, v[24:25]
	s_mov_b64 exec, -1
	v_cmp_lt_u32_e32 vcc, s36, v73
	s_mov_b64 exec, vcc
	ds_write_b32 v9, v73 offset:10496
	v_bfe_u32 v27, v73, 4, 4
	v_add_u32_e32 v6, 1, v6
	v_lshlrev_b32_e64 v28, v27, 1
	v_or_b32_e32 v7, v7, v28
	v_lshl_add_u32 v27, v27, 9, v8
	v_mov_b32_e32 v24, 0
	v_mov_b32_e32 v25, 0x200
	ds_or_b64 v27, v[24:25]
	s_mov_b64 exec, -1
	v_cmp_lt_u32_e32 vcc, s36, v74
	s_mov_b64 exec, vcc
	ds_write_b32 v9, v74 offset:10752
	v_bfe_u32 v27, v74, 4, 4
	v_add_u32_e32 v6, 1, v6
	v_lshlrev_b32_e64 v28, v27, 1
	v_or_b32_e32 v7, v7, v28
	v_lshl_add_u32 v27, v27, 9, v8
	v_mov_b32_e32 v24, 0
	v_mov_b32_e32 v25, 0x400
	ds_or_b64 v27, v[24:25]
	s_mov_b64 exec, -1
	v_cmp_lt_u32_e32 vcc, s36, v75
	s_mov_b64 exec, vcc
	ds_write_b32 v9, v75 offset:11008
	v_bfe_u32 v27, v75, 4, 4
	v_add_u32_e32 v6, 1, v6
	v_lshlrev_b32_e64 v28, v27, 1
	v_or_b32_e32 v7, v7, v28
	v_lshl_add_u32 v27, v27, 9, v8
	v_mov_b32_e32 v24, 0
	v_mov_b32_e32 v25, 0x800
	ds_or_b64 v27, v[24:25]
	s_mov_b64 exec, -1
	s_cmp_le_u32 s14, 44
	s_cbranch_scc1 .Lro_built
	v_cmp_lt_u32_e32 vcc, s36, v76
	s_mov_b64 exec, vcc
	ds_write_b32 v9, v76 offset:11264
	v_bfe_u32 v27, v76, 4, 4
	v_add_u32_e32 v6, 1, v6
	v_lshlrev_b32_e64 v28, v27, 1
	v_or_b32_e32 v7, v7, v28
	v_lshl_add_u32 v27, v27, 9, v8
	v_mov_b32_e32 v24, 0
	v_mov_b32_e32 v25, 0x1000
	ds_or_b64 v27, v[24:25]
	s_mov_b64 exec, -1
	v_cmp_lt_u32_e32 vcc, s36, v77
	s_mov_b64 exec, vcc
	ds_write_b32 v9, v77 offset:11520
	v_bfe_u32 v27, v77, 4, 4
	v_add_u32_e32 v6, 1, v6
	v_lshlrev_b32_e64 v28, v27, 1
	v_or_b32_e32 v7, v7, v28
	v_lshl_add_u32 v27, v27, 9, v8
	v_mov_b32_e32 v24, 0
	v_mov_b32_e32 v25, 0x2000
	ds_or_b64 v27, v[24:25]
	s_mov_b64 exec, -1
	v_cmp_lt_u32_e32 vcc, s36, v78
	s_mov_b64 exec, vcc
	ds_write_b32 v9, v78 offset:11776
	v_bfe_u32 v27, v78, 4, 4
	v_add_u32_e32 v6, 1, v6
	v_lshlrev_b32_e64 v28, v27, 1
	v_or_b32_e32 v7, v7, v28
	v_lshl_add_u32 v27, v27, 9, v8
	v_mov_b32_e32 v24, 0
	v_mov_b32_e32 v25, 0x4000
	ds_or_b64 v27, v[24:25]
	s_mov_b64 exec, -1
	v_cmp_lt_u32_e32 vcc, s36, v79
	s_mov_b64 exec, vcc
	ds_write_b32 v9, v79 offset:12032
	v_bfe_u32 v27, v79, 4, 4
	v_add_u32_e32 v6, 1, v6
	v_lshlrev_b32_e64 v28, v27, 1
	v_or_b32_e32 v7, v7, v28
	v_lshl_add_u32 v27, v27, 9, v8
	v_mov_b32_e32 v24, 0
	v_mov_b32_e32 v25, 0x8000
	ds_or_b64 v27, v[24:25]
	s_mov_b64 exec, -1
	s_cmp_le_u32 s14, 48
	s_cbranch_scc1 .Lro_built
	v_cmp_lt_u32_e32 vcc, s36, v80
	s_mov_b64 exec, vcc
	ds_write_b32 v9, v80 offset:12288
	v_bfe_u32 v27, v80, 4, 4
	v_add_u32_e32 v6, 1, v6
	v_lshlrev_b32_e64 v28, v27, 1
	v_or_b32_e32 v7, v7, v28
	v_lshl_add_u32 v27, v27, 9, v8
	v_mov_b32_e32 v24, 0
	v_mov_b32_e32 v25, 0x10000
	ds_or_b64 v27, v[24:25]
	s_mov_b64 exec, -1
	v_cmp_lt_u32_e32 vcc, s36, v81
	s_mov_b64 exec, vcc
	ds_write_b32 v9, v81 offset:12544
	v_bfe_u32 v27, v81, 4, 4
	v_add_u32_e32 v6, 1, v6
	v_lshlrev_b32_e64 v28, v27, 1
	v_or_b32_e32 v7, v7, v28
	v_lshl_add_u32 v27, v27, 9, v8
	v_mov_b32_e32 v24, 0
	v_mov_b32_e32 v25, 0x20000
	ds_or_b64 v27, v[24:25]
	s_mov_b64 exec, -1
	v_cmp_lt_u32_e32 vcc, s36, v82
	s_mov_b64 exec, vcc
	ds_write_b32 v9, v82 offset:12800
	v_bfe_u32 v27, v82, 4, 4
	v_add_u32_e32 v6, 1, v6
	v_lshlrev_b32_e64 v28, v27, 1
	v_or_b32_e32 v7, v7, v28
	v_lshl_add_u32 v27, v27, 9, v8
	v_mov_b32_e32 v24, 0
	v_mov_b32_e32 v25, 0x40000
	ds_or_b64 v27, v[24:25]
	s_mov_b64 exec, -1
	v_cmp_lt_u32_e32 vcc, s36, v83
	s_mov_b64 exec, vcc
	ds_write_b32 v9, v83 offset:13056
	v_bfe_u32 v27, v83, 4, 4
	v_add_u32_e32 v6, 1, v6
	v_lshlrev_b32_e64 v28, v27, 1
	v_or_b32_e32 v7, v7, v28
	v_lshl_add_u32 v27, v27, 9, v8
	v_mov_b32_e32 v24, 0
	v_mov_b32_e32 v25, 0x80000
	ds_or_b64 v27, v[24:25]
	s_mov_b64 exec, -1
	s_cmp_le_u32 s14, 52
	s_cbranch_scc1 .Lro_built
	v_cmp_lt_u32_e32 vcc, s36, v84
	s_mov_b64 exec, vcc
	ds_write_b32 v9, v84 offset:13312
	v_bfe_u32 v27, v84, 4, 4
	v_add_u32_e32 v6, 1, v6
	v_lshlrev_b32_e64 v28, v27, 1
	v_or_b32_e32 v7, v7, v28
	v_lshl_add_u32 v27, v27, 9, v8
	v_mov_b32_e32 v24, 0
	v_mov_b32_e32 v25, 0x100000
	ds_or_b64 v27, v[24:25]
	s_mov_b64 exec, -1
	v_cmp_lt_u32_e32 vcc, s36, v85
	s_mov_b64 exec, vcc
	ds_write_b32 v9, v85 offset:13568
	v_bfe_u32 v27, v85, 4, 4
	v_add_u32_e32 v6, 1, v6
	v_lshlrev_b32_e64 v28, v27, 1
	v_or_b32_e32 v7, v7, v28
	v_lshl_add_u32 v27, v27, 9, v8
	v_mov_b32_e32 v24, 0
	v_mov_b32_e32 v25, 0x200000
	ds_or_b64 v27, v[24:25]
	s_mov_b64 exec, -1
	v_cmp_lt_u32_e32 vcc, s36, v86
	s_mov_b64 exec, vcc
	ds_write_b32 v9, v86 offset:13824
	v_bfe_u32 v27, v86, 4, 4
	v_add_u32_e32 v6, 1, v6
	v_lshlrev_b32_e64 v28, v27, 1
	v_or_b32_e32 v7, v7, v28
	v_lshl_add_u32 v27, v27, 9, v8
	v_mov_b32_e32 v24, 0
	v_mov_b32_e32 v25, 0x400000
	ds_or_b64 v27, v[24:25]
	s_mov_b64 exec, -1
	v_cmp_lt_u32_e32 vcc, s36, v87
	s_mov_b64 exec, vcc
	ds_write_b32 v9, v87 offset:14080
	v_bfe_u32 v27, v87, 4, 4
	v_add_u32_e32 v6, 1, v6
	v_lshlrev_b32_e64 v28, v27, 1
	v_or_b32_e32 v7, v7, v28
	v_lshl_add_u32 v27, v27, 9, v8
	v_mov_b32_e32 v24, 0
	v_mov_b32_e32 v25, 0x800000
	ds_or_b64 v27, v[24:25]
	s_mov_b64 exec, -1
	s_cmp_le_u32 s14, 56
	s_cbranch_scc1 .Lro_built
	v_cmp_lt_u32_e32 vcc, s36, v88
	s_mov_b64 exec, vcc
	ds_write_b32 v9, v88 offset:14336
	v_bfe_u32 v27, v88, 4, 4
	v_add_u32_e32 v6, 1, v6
	v_lshlrev_b32_e64 v28, v27, 1
	v_or_b32_e32 v7, v7, v28
	v_lshl_add_u32 v27, v27, 9, v8
	v_mov_b32_e32 v24, 0
	v_mov_b32_e32 v25, 0x1000000
	ds_or_b64 v27, v[24:25]
	s_mov_b64 exec, -1
	v_cmp_lt_u32_e32 vcc, s36, v89
	s_mov_b64 exec, vcc
	ds_write_b32 v9, v89 offset:14592
	v_bfe_u32 v27, v89, 4, 4
	v_add_u32_e32 v6, 1, v6
	v_lshlrev_b32_e64 v28, v27, 1
	v_or_b32_e32 v7, v7, v28
	v_lshl_add_u32 v27, v27, 9, v8
	v_mov_b32_e32 v24, 0
	v_mov_b32_e32 v25, 0x2000000
	ds_or_b64 v27, v[24:25]
	s_mov_b64 exec, -1
	v_cmp_lt_u32_e32 vcc, s36, v90
	s_mov_b64 exec, vcc
	ds_write_b32 v9, v90 offset:14848
	v_bfe_u32 v27, v90, 4, 4
	v_add_u32_e32 v6, 1, v6
	v_lshlrev_b32_e64 v28, v27, 1
	v_or_b32_e32 v7, v7, v28
	v_lshl_add_u32 v27, v27, 9, v8
	v_mov_b32_e32 v24, 0
	v_mov_b32_e32 v25, 0x4000000
	ds_or_b64 v27, v[24:25]
	s_mov_b64 exec, -1
	v_cmp_lt_u32_e32 vcc, s36, v91
	s_mov_b64 exec, vcc
	ds_write_b32 v9, v91 offset:15104
	v_bfe_u32 v27, v91, 4, 4
	v_add_u32_e32 v6, 1, v6
	v_lshlrev_b32_e64 v28, v27, 1
	v_or_b32_e32 v7, v7, v28
	v_lshl_add_u32 v27, v27, 9, v8
	v_mov_b32_e32 v24, 0
	v_mov_b32_e32 v25, 0x8000000
	ds_or_b64 v27, v[24:25]
	s_mov_b64 exec, -1
	s_cmp_le_u32 s14, 60
	s_cbranch_scc1 .Lro_built
	v_cmp_lt_u32_e32 vcc, s36, v92
	s_mov_b64 exec, vcc
	ds_write_b32 v9, v92 offset:15360
	v_bfe_u32 v27, v92, 4, 4
	v_add_u32_e32 v6, 1, v6
	v_lshlrev_b32_e64 v28, v27, 1
	v_or_b32_e32 v7, v7, v28
	v_lshl_add_u32 v27, v27, 9, v8
	v_mov_b32_e32 v24, 0
	v_mov_b32_e32 v25, 0x10000000
	ds_or_b64 v27, v[24:25]
	s_mov_b64 exec, -1
	v_cmp_lt_u32_e32 vcc, s36, v93
	s_mov_b64 exec, vcc
	ds_write_b32 v9, v93 offset:15616
	v_bfe_u32 v27, v93, 4, 4
	v_add_u32_e32 v6, 1, v6
	v_lshlrev_b32_e64 v28, v27, 1
	v_or_b32_e32 v7, v7, v28
	v_lshl_add_u32 v27, v27, 9, v8
	v_mov_b32_e32 v24, 0
	v_mov_b32_e32 v25, 0x20000000
	ds_or_b64 v27, v[24:25]
	s_mov_b64 exec, -1
	v_cmp_lt_u32_e32 vcc, s36, v94
	s_mov_b64 exec, vcc
	ds_write_b32 v9, v94 offset:15872
	v_bfe_u32 v27, v94, 4, 4
	v_add_u32_e32 v6, 1, v6
	v_lshlrev_b32_e64 v28, v27, 1
	v_or_b32_e32 v7, v7, v28
	v_lshl_add_u32 v27, v27, 9, v8
	v_mov_b32_e32 v24, 0
	v_mov_b32_e32 v25, 0x40000000
	ds_or_b64 v27, v[24:25]
	s_mov_b64 exec, -1
	v_cmp_lt_u32_e32 vcc, s36, v95
	s_mov_b64 exec, vcc
	ds_write_b32 v9, v95 offset:16128
	v_bfe_u32 v27, v95, 4, 4
	v_add_u32_e32 v6, 1, v6
	v_lshlrev_b32_e64 v28, v27, 1
	v_or_b32_e32 v7, v7, v28
	v_lshl_add_u32 v27, v27, 9, v8
	v_mov_b32_e32 v24, 0
	v_mov_b32_e32 v25, 0x80000000
	ds_or_b64 v27, v[24:25]
	s_mov_b64 exec, -1

.Lro_round:
	s_sub_u32 s34, s14, s18
	s_mul_i32 s32, s18, 7
	s_and_b32 s32, s32, 15
	v_cmp_gt_u32_e64 s[24:25], s34, v6
	v_cmp_eq_u32_e32 vcc, s32, v2
	v_mov_b32_e32 v12, 0
	s_nop 1
	v_cndmask_b32_dpp v13, v12, v11, vcc row_ror:1 row_mask:0xf bank_mask:0xf
	v_bfi_b32 v14, v13, 0, v7
	v_cmp_ne_u32_e64 s[26:27], 0, v14
	v_not_b32_e32 v15, v13
	v_cndmask_b32_e64 v16, v7, v15, s[24:25]
	v_cndmask_b32_e64 v17, v16, v14, s[26:27]
	v_ffbl_b32_e32 v20, v17
	v_lshlrev_b32_e64 v21, v20, 1
	v_or_b32_e32 v12, v13, v21
	s_nop 1
	v_cndmask_b32_dpp v13, v12, v11, vcc row_ror:1 row_mask:0xf bank_mask:0xf
	v_bfi_b32 v14, v13, 0, v7
	v_cmp_ne_u32_e64 s[26:27], 0, v14
	v_not_b32_e32 v15, v13
	v_cndmask_b32_e64 v16, v7, v15, s[24:25]
	v_cndmask_b32_e64 v17, v16, v14, s[26:27]
	v_ffbl_b32_e32 v20, v17
	v_lshlrev_b32_e64 v21, v20, 1
	v_or_b32_e32 v12, v13, v21
	s_nop 1
	v_cndmask_b32_dpp v13, v12, v11, vcc row_ror:1 row_mask:0xf bank_mask:0xf
	v_bfi_b32 v14, v13, 0, v7
	v_cmp_ne_u32_e64 s[26:27], 0, v14
	v_not_b32_e32 v15, v13
	v_cndmask_b32_e64 v16, v7, v15, s[24:25]
	v_cndmask_b32_e64 v17, v16, v14, s[26:27]
	v_ffbl_b32_e32 v20, v17
	v_lshlrev_b32_e64 v21, v20, 1
	v_or_b32_e32 v12, v13, v21
	s_nop 1
	v_cndmask_b32_dpp v13, v12, v11, vcc row_ror:1 row_mask:0xf bank_mask:0xf
	v_bfi_b32 v14, v13, 0, v7
	v_cmp_ne_u32_e64 s[26:27], 0, v14
	v_not_b32_e32 v15, v13
	v_cndmask_b32_e64 v16, v7, v15, s[24:25]
	v_cndmask_b32_e64 v17, v16, v14, s[26:27]
	v_ffbl_b32_e32 v20, v17
	v_lshlrev_b32_e64 v21, v20, 1
	v_or_b32_e32 v12, v13, v21
	s_nop 1
	v_cndmask_b32_dpp v13, v12, v11, vcc row_ror:1 row_mask:0xf bank_mask:0xf
	v_bfi_b32 v14, v13, 0, v7
	v_cmp_ne_u32_e64 s[26:27], 0, v14
	v_not_b32_e32 v15, v13
	v_cndmask_b32_e64 v16, v7, v15, s[24:25]
	v_cndmask_b32_e64 v17, v16, v14, s[26:27]
	v_ffbl_b32_e32 v20, v17
	v_lshlrev_b32_e64 v21, v20, 1
	v_or_b32_e32 v12, v13, v21
	s_nop 1
	v_cndmask_b32_dpp v13, v12, v11, vcc row_ror:1 row_mask:0xf bank_mask:0xf
	v_bfi_b32 v14, v13, 0, v7
	v_cmp_ne_u32_e64 s[26:27], 0, v14
	v_not_b32_e32 v15, v13
	v_cndmask_b32_e64 v16, v7, v15, s[24:25]
	v_cndmask_b32_e64 v17, v16, v14, s[26:27]
	v_ffbl_b32_e32 v20, v17
	v_lshlrev_b32_e64 v21, v20, 1
	v_or_b32_e32 v12, v13, v21
	s_nop 1
	v_cndmask_b32_dpp v13, v12, v11, vcc row_ror:1 row_mask:0xf bank_mask:0xf
	v_bfi_b32 v14, v13, 0, v7
	v_cmp_ne_u32_e64 s[26:27], 0, v14
	v_not_b32_e32 v15, v13
	v_cndmask_b32_e64 v16, v7, v15, s[24:25]
	v_cndmask_b32_e64 v17, v16, v14, s[26:27]
	v_ffbl_b32_e32 v20, v17
	v_lshlrev_b32_e64 v21, v20, 1
	v_or_b32_e32 v12, v13, v21
	s_nop 1
	v_cndmask_b32_dpp v13, v12, v11, vcc row_ror:1 row_mask:0xf bank_mask:0xf
	v_bfi_b32 v14, v13, 0, v7
	v_cmp_ne_u32_e64 s[26:27], 0, v14
	v_not_b32_e32 v15, v13
	v_cndmask_b32_e64 v16, v7, v15, s[24:25]
	v_cndmask_b32_e64 v17, v16, v14, s[26:27]
	v_ffbl_b32_e32 v20, v17
	v_lshlrev_b32_e64 v21, v20, 1
	v_or_b32_e32 v12, v13, v21
	s_nop 1
	v_cndmask_b32_dpp v13, v12, v11, vcc row_ror:1 row_mask:0xf bank_mask:0xf
	v_bfi_b32 v14, v13, 0, v7
	v_cmp_ne_u32_e64 s[26:27], 0, v14
	v_not_b32_e32 v15, v13
	v_cndmask_b32_e64 v16, v7, v15, s[24:25]
	v_cndmask_b32_e64 v17, v16, v14, s[26:27]
	v_ffbl_b32_e32 v20, v17
	v_lshlrev_b32_e64 v21, v20, 1
	v_or_b32_e32 v12, v13, v21
	s_nop 1
	v_cndmask_b32_dpp v13, v12, v11, vcc row_ror:1 row_mask:0xf bank_mask:0xf
	v_bfi_b32 v14, v13, 0, v7
	v_cmp_ne_u32_e64 s[26:27], 0, v14
	v_not_b32_e32 v15, v13
	v_cndmask_b32_e64 v16, v7, v15, s[24:25]
	v_cndmask_b32_e64 v17, v16, v14, s[26:27]
	v_ffbl_b32_e32 v20, v17
	v_lshlrev_b32_e64 v21, v20, 1
	v_or_b32_e32 v12, v13, v21
	s_nop 1
	v_cndmask_b32_dpp v13, v12, v11, vcc row_ror:1 row_mask:0xf bank_mask:0xf
	v_bfi_b32 v14, v13, 0, v7
	v_cmp_ne_u32_e64 s[26:27], 0, v14
	v_not_b32_e32 v15, v13
	v_cndmask_b32_e64 v16, v7, v15, s[24:25]
	v_cndmask_b32_e64 v17, v16, v14, s[26:27]
	v_ffbl_b32_e32 v20, v17
	v_lshlrev_b32_e64 v21, v20, 1
	v_or_b32_e32 v12, v13, v21
	s_nop 1
	v_cndmask_b32_dpp v13, v12, v11, vcc row_ror:1 row_mask:0xf bank_mask:0xf
	v_bfi_b32 v14, v13, 0, v7
	v_cmp_ne_u32_e64 s[26:27], 0, v14
	v_not_b32_e32 v15, v13
	v_cndmask_b32_e64 v16, v7, v15, s[24:25]
	v_cndmask_b32_e64 v17, v16, v14, s[26:27]
	v_ffbl_b32_e32 v20, v17
	v_lshlrev_b32_e64 v21, v20, 1
	v_or_b32_e32 v12, v13, v21
	s_nop 1
	v_cndmask_b32_dpp v13, v12, v11, vcc row_ror:1 row_mask:0xf bank_mask:0xf
	v_bfi_b32 v14, v13, 0, v7
	v_cmp_ne_u32_e64 s[26:27], 0, v14
	v_not_b32_e32 v15, v13
	v_cndmask_b32_e64 v16, v7, v15, s[24:25]
	v_cndmask_b32_e64 v17, v16, v14, s[26:27]
	v_ffbl_b32_e32 v20, v17
	v_lshlrev_b32_e64 v21, v20, 1
	v_or_b32_e32 v12, v13, v21
	s_nop 1
	v_cndmask_b32_dpp v13, v12, v11, vcc row_ror:1 row_mask:0xf bank_mask:0xf
	v_bfi_b32 v14, v13, 0, v7
	v_cmp_ne_u32_e64 s[26:27], 0, v14
	v_not_b32_e32 v15, v13
	v_cndmask_b32_e64 v16, v7, v15, s[24:25]
	v_cndmask_b32_e64 v17, v16, v14, s[26:27]
	v_ffbl_b32_e32 v20, v17
	v_lshlrev_b32_e64 v21, v20, 1
	v_or_b32_e32 v12, v13, v21
	s_nop 1
	v_cndmask_b32_dpp v13, v12, v11, vcc row_ror:1 row_mask:0xf bank_mask:0xf
	v_bfi_b32 v14, v13, 0, v7
	v_cmp_ne_u32_e64 s[26:27], 0, v14
	v_not_b32_e32 v15, v13
	v_cndmask_b32_e64 v16, v7, v15, s[24:25]
	v_cndmask_b32_e64 v17, v16, v14, s[26:27]
	v_ffbl_b32_e32 v20, v17
	v_lshlrev_b32_e64 v21, v20, 1
	v_or_b32_e32 v12, v13, v21
	s_nop 1
	v_cndmask_b32_dpp v13, v12, v11, vcc row_ror:1 row_mask:0xf bank_mask:0xf
	v_bfi_b32 v14, v13, 0, v7
	v_cmp_ne_u32_e64 s[26:27], 0, v14
	v_not_b32_e32 v15, v13
	v_cndmask_b32_e64 v16, v7, v15, s[24:25]
	v_cndmask_b32_e64 v17, v16, v14, s[26:27]
	v_ffbl_b32_e32 v20, v17
	v_lshlrev_b32_e64 v21, v20, 1
	v_or_b32_e32 v12, v13, v21
	s_orn2_b64 s[28:29], s[26:27], s[24:25]
	v_lshlrev_b32_e32 v29, 4, v20
	s_and_saveexec_b64 s[22:23], s[28:29]
	s_cbranch_execz .Lro_nopop
	v_lshl_add_u32 v30, v20, 9, v8
	ds_read_b64 v[24:25], v30
	s_waitcnt lgkmcnt(0)
	v_ffbl_b32_e32 v26, v24
	v_ffbl_b32_e32 v27, v25
	v_add_u32_e32 v27, 32, v27
	v_min_u32_e32 v28, v26, v27
	v_lshl_add_u32 v31, v28, 8, v9
	ds_read_b32 v29, v31
	v_lshlrev_b64 v[26:27], v28, 1
	v_bfi_b32 v24, v26, 0, v24
	v_bfi_b32 v25, v27, 0, v25
	ds_write_b64 v30, v[24:25]
	v_or_b32_e32 v24, v24, v25
	v_cmp_eq_u32_e32 vcc, 0, v24
	v_bfi_b32 v27, v21, 0, v7
	v_subrev_u32_e32 v6, 1, v6
	s_nop 0
	v_cndmask_b32_e32 v7, v7, v27, vcc
	s_waitcnt lgkmcnt(0)
